# grid barrier: non-last workgroups poll the top-level arrival counter instead of the generation word (one atomic round trip earlier); on top of early L1 invalidate and the combine-phase changes
# speedup vs baseline: 1.0284x; 1.0024x over previous
.LBB0_239:
	s_or_b64 exec, exec, s[2:3]
	v_cvt_f32_u32_e32 v6, v4
	s_waitcnt vmcnt(0)
	v_readfirstlane_b32 s2, v5
	v_sub_u32_e32 v5, 0, v4
	v_rcp_iflag_f32_e32 v6, v6
	v_add_u32_e32 v7, s2, v3
	v_mul_f32_e32 v6, 0x4f7ffffe, v6
	v_cvt_u32_f32_e32 v6, v6
	v_mul_lo_u32 v3, v5, v6
	v_mul_hi_u32 v3, v6, v3
	v_add_u32_e32 v3, v6, v3
	v_mul_hi_u32 v3, v7, v3
	v_mul_lo_u32 v5, v3, v4
	v_sub_u32_e32 v5, v7, v5
	v_add_u32_e32 v6, 1, v3
	v_cmp_ge_u32_e32 vcc, v5, v4
	s_nop 1
	v_cndmask_b32_e32 v3, v3, v6, vcc
	v_sub_u32_e32 v6, v5, v4
	v_cndmask_b32_e32 v5, v5, v6, vcc
	v_add_u32_e32 v6, 1, v3
	v_cmp_ge_u32_e32 vcc, v5, v4
	v_add_u32_e32 v5, 1, v7
	s_nop 0
	v_cndmask_b32_e32 v3, v3, v6, vcc
	v_mul_lo_u32 v6, v4, v3
	v_add_u32_e32 v4, v6, v4
	v_cmp_ne_u32_e32 vcc, v5, v4
	s_and_saveexec_b64 s[2:3], vcc
	s_xor_b64 s[2:3], exec, s[2:3]
	s_cbranch_execz .LBB0_253
	v_readlane_b32 s6, v255, 9
	s_waitcnt lgkmcnt(0)
	v_mov_b32_e32 v2, 0x20164
	ds_read_b32 v2, v2
	s_waitcnt lgkmcnt(0)
	v_add_u32_e32 v3, 1, v3
	v_mul_lo_u32 v3, v3, v2
	v_mov_b32_e32 v2, 0x3000
	v_readlane_b32 s7, v255, 10
	s_add_u32 s8, s6, 0x3400
	s_addc_u32 s9, s7, 0
	s_nop 2
	global_load_dword v2, v2, s[6:7] offset:1024 sc1
	s_waitcnt vmcnt(0)
	v_cmp_lt_u32_e32 vcc, v2, v3
	s_and_saveexec_b64 s[6:7], vcc
	s_cbranch_execz .LBB0_252
	s_mov_b32 s10, 1
	s_mov_b64 s[14:15], 0
	v_mov_b32_e32 v2, 0
	s_branch .LBB0_243

.LBB0_247:
	global_load_dword v4, v2, s[8:9] sc1
	s_add_i32 s10, s10, 1
	s_mov_b64 s[60:61], -1
	s_waitcnt vmcnt(0)
	v_cmp_ge_u32_e32 vcc, v4, v3
	s_orn2_b64 s[28:29], vcc, exec
	s_branch .LBB0_242

.LBB0_383:
	s_or_b64 exec, exec, s[2:3]
	v_cvt_f32_u32_e32 v6, v4
	s_waitcnt vmcnt(0)
	v_readfirstlane_b32 s2, v5
	v_sub_u32_e32 v5, 0, v4
	v_rcp_iflag_f32_e32 v6, v6
	v_add_u32_e32 v7, s2, v3
	v_mul_f32_e32 v6, 0x4f7ffffe, v6
	v_cvt_u32_f32_e32 v6, v6
	v_mul_lo_u32 v3, v5, v6
	v_mul_hi_u32 v3, v6, v3
	v_add_u32_e32 v3, v6, v3
	v_mul_hi_u32 v3, v7, v3
	v_mul_lo_u32 v5, v3, v4
	v_sub_u32_e32 v5, v7, v5
	v_add_u32_e32 v6, 1, v3
	v_cmp_ge_u32_e32 vcc, v5, v4
	s_nop 1
	v_cndmask_b32_e32 v3, v3, v6, vcc
	v_sub_u32_e32 v6, v5, v4
	v_cndmask_b32_e32 v5, v5, v6, vcc
	v_add_u32_e32 v6, 1, v3
	v_cmp_ge_u32_e32 vcc, v5, v4
	v_add_u32_e32 v5, 1, v7
	s_nop 0
	v_cndmask_b32_e32 v3, v3, v6, vcc
	v_mul_lo_u32 v6, v4, v3
	v_add_u32_e32 v4, v6, v4
	v_cmp_ne_u32_e32 vcc, v5, v4
	s_and_saveexec_b64 s[2:3], vcc
	s_xor_b64 s[2:3], exec, s[2:3]
	s_cbranch_execz .LBB0_397
	v_readlane_b32 s6, v255, 9
	s_waitcnt lgkmcnt(0)
	v_mov_b32_e32 v2, 0x20164
	ds_read_b32 v2, v2
	s_waitcnt lgkmcnt(0)
	v_add_u32_e32 v3, 1, v3
	v_mul_lo_u32 v3, v3, v2
	v_mov_b32_e32 v2, 0x3000
	v_readlane_b32 s7, v255, 10
	s_add_u32 s8, s6, 0x3400
	s_addc_u32 s9, s7, 0
	s_nop 2
	global_load_dword v2, v2, s[6:7] offset:1024 sc1
	s_waitcnt vmcnt(0)
	v_cmp_lt_u32_e32 vcc, v2, v3
	s_and_saveexec_b64 s[6:7], vcc
	s_cbranch_execz .LBB0_396
	s_mov_b32 s10, 1
	s_mov_b64 s[18:19], 0
	v_mov_b32_e32 v2, 0
	s_branch .LBB0_387

.LBB0_391:
	global_load_dword v4, v2, s[8:9] sc1
	s_add_i32 s10, s10, 1
	s_mov_b64 s[62:63], -1
	s_waitcnt vmcnt(0)
	v_cmp_ge_u32_e32 vcc, v4, v3
	s_orn2_b64 s[60:61], vcc, exec
	s_branch .LBB0_386

.LBB0_838:
	s_or_b64 exec, exec, s[6:7]
	v_cvt_f32_u32_e32 v6, v4
	s_waitcnt vmcnt(0)
	v_readfirstlane_b32 s6, v5
	v_sub_u32_e32 v5, 0, v4
	v_rcp_iflag_f32_e32 v6, v6
	v_add_u32_e32 v7, s6, v3
	v_mul_f32_e32 v6, 0x4f7ffffe, v6
	v_cvt_u32_f32_e32 v6, v6
	v_mul_lo_u32 v3, v5, v6
	v_mul_hi_u32 v3, v6, v3
	v_add_u32_e32 v3, v6, v3
	v_mul_hi_u32 v3, v7, v3
	v_mul_lo_u32 v5, v3, v4
	v_sub_u32_e32 v5, v7, v5
	v_add_u32_e32 v6, 1, v3
	v_cmp_ge_u32_e32 vcc, v5, v4
	s_nop 1
	v_cndmask_b32_e32 v3, v3, v6, vcc
	v_sub_u32_e32 v6, v5, v4
	v_cndmask_b32_e32 v5, v5, v6, vcc
	v_add_u32_e32 v6, 1, v3
	v_cmp_ge_u32_e32 vcc, v5, v4
	v_add_u32_e32 v5, 1, v7
	s_nop 0
	v_cndmask_b32_e32 v3, v3, v6, vcc
	v_mul_lo_u32 v6, v4, v3
	v_add_u32_e32 v4, v6, v4
	v_cmp_ne_u32_e32 vcc, v5, v4
	s_and_saveexec_b64 s[6:7], vcc
	s_xor_b64 s[6:7], exec, s[6:7]
	s_cbranch_execz .LBB0_852
	v_readlane_b32 s8, v255, 9
	s_waitcnt lgkmcnt(0)
	v_mov_b32_e32 v2, 0x20164
	ds_read_b32 v2, v2
	s_waitcnt lgkmcnt(0)
	v_add_u32_e32 v3, 1, v3
	v_mul_lo_u32 v3, v3, v2
	v_mov_b32_e32 v2, 0x3000
	v_readlane_b32 s9, v255, 10
	s_add_u32 s18, s8, 0x3400
	s_addc_u32 s19, s9, 0
	s_nop 2
	global_load_dword v2, v2, s[8:9] offset:1024 sc1
	s_waitcnt vmcnt(0)
	v_cmp_lt_u32_e32 vcc, v2, v3
	s_and_saveexec_b64 s[16:17], vcc
	s_cbranch_execz .LBB0_851
	s_mov_b32 s8, 1
	s_mov_b64 s[20:21], 0
	v_mov_b32_e32 v2, 0
	s_branch .LBB0_842

.LBB0_846:
	global_load_dword v4, v2, s[18:19] sc1
	s_add_i32 s8, s8, 1
	s_mov_b64 s[26:27], -1
	s_waitcnt vmcnt(0)
	v_cmp_ge_u32_e32 vcc, v4, v3
	s_orn2_b64 s[24:25], vcc, exec
	s_branch .LBB0_841

.LBB0_918:
	s_or_b64 exec, exec, s[6:7]
	v_cvt_f32_u32_e32 v6, v4
	s_waitcnt vmcnt(0)
	v_readfirstlane_b32 s6, v5
	v_sub_u32_e32 v5, 0, v4
	v_rcp_iflag_f32_e32 v6, v6
	v_add_u32_e32 v7, s6, v3
	v_mul_f32_e32 v6, 0x4f7ffffe, v6
	v_cvt_u32_f32_e32 v6, v6
	v_mul_lo_u32 v3, v5, v6
	v_mul_hi_u32 v3, v6, v3
	v_add_u32_e32 v3, v6, v3
	v_mul_hi_u32 v3, v7, v3
	v_mul_lo_u32 v5, v3, v4
	v_sub_u32_e32 v5, v7, v5
	v_add_u32_e32 v6, 1, v3
	v_cmp_ge_u32_e32 vcc, v5, v4
	s_nop 1
	v_cndmask_b32_e32 v3, v3, v6, vcc
	v_sub_u32_e32 v6, v5, v4
	v_cndmask_b32_e32 v5, v5, v6, vcc
	v_add_u32_e32 v6, 1, v3
	v_cmp_ge_u32_e32 vcc, v5, v4
	v_add_u32_e32 v5, 1, v7
	s_nop 0
	v_cndmask_b32_e32 v3, v3, v6, vcc
	v_mul_lo_u32 v6, v4, v3
	v_add_u32_e32 v4, v6, v4
	v_cmp_ne_u32_e32 vcc, v5, v4
	s_and_saveexec_b64 s[6:7], vcc
	s_xor_b64 s[6:7], exec, s[6:7]
	s_cbranch_execz .LBB0_932
	v_readlane_b32 s8, v255, 9
	s_waitcnt lgkmcnt(0)
	v_mov_b32_e32 v2, 0x20164
	ds_read_b32 v2, v2
	s_waitcnt lgkmcnt(0)
	v_add_u32_e32 v3, 1, v3
	v_mul_lo_u32 v3, v3, v2
	v_mov_b32_e32 v2, 0x3000
	v_readlane_b32 s9, v255, 10
	s_add_u32 s14, s8, 0x3400
	s_addc_u32 s15, s9, 0
	s_nop 2
	global_load_dword v2, v2, s[8:9] offset:1024 sc1
	s_waitcnt vmcnt(0)
	v_cmp_lt_u32_e32 vcc, v2, v3
	s_and_saveexec_b64 s[8:9], vcc
	s_cbranch_execz .LBB0_931
	s_mov_b32 s10, 1
	s_mov_b64 s[16:17], 0
	v_mov_b32_e32 v2, 0
	s_branch .LBB0_922

.LBB0_926:
	global_load_dword v4, v2, s[14:15] sc1
	s_add_i32 s10, s10, 1
	s_mov_b64 s[22:23], -1
	s_waitcnt vmcnt(0)
	v_cmp_ge_u32_e32 vcc, v4, v3
	s_orn2_b64 s[20:21], vcc, exec
	s_branch .LBB0_921

.LBB0_998:
	s_or_b64 exec, exec, s[6:7]
	v_cvt_f32_u32_e32 v70, v68
	s_waitcnt vmcnt(0)
	v_readfirstlane_b32 s6, v69
	v_sub_u32_e32 v69, 0, v68
	v_rcp_iflag_f32_e32 v70, v70
	v_add_u32_e32 v71, s6, v67
	v_mul_f32_e32 v70, 0x4f7ffffe, v70
	v_cvt_u32_f32_e32 v70, v70
	v_mul_lo_u32 v67, v69, v70
	v_mul_hi_u32 v67, v70, v67
	v_add_u32_e32 v67, v70, v67
	v_mul_hi_u32 v67, v71, v67
	v_mul_lo_u32 v69, v67, v68
	v_sub_u32_e32 v69, v71, v69
	v_add_u32_e32 v70, 1, v67
	v_cmp_ge_u32_e32 vcc, v69, v68
	s_nop 1
	v_cndmask_b32_e32 v67, v67, v70, vcc
	v_sub_u32_e32 v70, v69, v68
	v_cndmask_b32_e32 v69, v69, v70, vcc
	v_add_u32_e32 v70, 1, v67
	v_cmp_ge_u32_e32 vcc, v69, v68
	v_add_u32_e32 v69, 1, v71
	s_nop 0
	v_cndmask_b32_e32 v67, v67, v70, vcc
	v_mul_lo_u32 v70, v68, v67
	v_add_u32_e32 v68, v70, v68
	v_cmp_ne_u32_e32 vcc, v69, v68
	s_and_saveexec_b64 s[6:7], vcc
	s_xor_b64 s[6:7], exec, s[6:7]
	s_cbranch_execz .LBB0_1012
	v_readlane_b32 s8, v255, 9
	s_waitcnt lgkmcnt(0)
	v_mov_b32_e32 v66, 0x20164
	ds_read_b32 v66, v66
	s_waitcnt lgkmcnt(0)
	v_add_u32_e32 v67, 1, v67
	v_mul_lo_u32 v67, v67, v66
	v_mov_b32_e32 v66, 0x3000
	v_readlane_b32 s9, v255, 10
	s_add_u32 s10, s8, 0x3400
	s_addc_u32 s11, s9, 0
	s_nop 2
	global_load_dword v66, v66, s[8:9] offset:1024 sc1
	s_waitcnt vmcnt(0)
	v_cmp_lt_u32_e32 vcc, v66, v67
	s_and_saveexec_b64 s[8:9], vcc
	s_cbranch_execz .LBB0_1011
	s_mov_b32 s22, 1
	s_mov_b64 s[12:13], 0
	v_mov_b32_e32 v66, 0
	s_branch .LBB0_1002

.LBB0_1006:
	global_load_dword v68, v66, s[10:11] sc1
	s_add_i32 s22, s22, 1
	s_mov_b64 s[18:19], -1
	s_waitcnt vmcnt(0)
	v_cmp_ge_u32_e32 vcc, v68, v67
	s_orn2_b64 s[16:17], vcc, exec
	s_branch .LBB0_1001

.LBB0_1138:
	s_or_b64 exec, exec, s[4:5]
	v_cvt_f32_u32_e32 v6, v4
	s_waitcnt vmcnt(0)
	v_readfirstlane_b32 s4, v5
	v_sub_u32_e32 v5, 0, v4
	v_rcp_iflag_f32_e32 v6, v6
	v_add_u32_e32 v7, s4, v3
	v_mul_f32_e32 v6, 0x4f7ffffe, v6
	v_cvt_u32_f32_e32 v6, v6
	v_mul_lo_u32 v3, v5, v6
	v_mul_hi_u32 v3, v6, v3
	v_add_u32_e32 v3, v6, v3
	v_mul_hi_u32 v3, v7, v3
	v_mul_lo_u32 v5, v3, v4
	v_sub_u32_e32 v5, v7, v5
	v_add_u32_e32 v6, 1, v3
	v_cmp_ge_u32_e32 vcc, v5, v4
	s_nop 1
	v_cndmask_b32_e32 v3, v3, v6, vcc
	v_sub_u32_e32 v6, v5, v4
	v_cndmask_b32_e32 v5, v5, v6, vcc
	v_add_u32_e32 v6, 1, v3
	v_cmp_ge_u32_e32 vcc, v5, v4
	v_add_u32_e32 v5, 1, v7
	s_nop 0
	v_cndmask_b32_e32 v3, v3, v6, vcc
	v_mul_lo_u32 v6, v4, v3
	v_add_u32_e32 v4, v6, v4
	v_cmp_ne_u32_e32 vcc, v5, v4
	s_and_saveexec_b64 s[4:5], vcc
	s_xor_b64 s[4:5], exec, s[4:5]
	s_cbranch_execz .LBB0_1152
	v_readlane_b32 s6, v255, 9
	s_waitcnt lgkmcnt(0)
	v_mov_b32_e32 v2, 0x20164
	ds_read_b32 v2, v2
	s_waitcnt lgkmcnt(0)
	v_add_u32_e32 v3, 1, v3
	v_mul_lo_u32 v3, v3, v2
	v_mov_b32_e32 v2, 0x3000
	v_readlane_b32 s7, v255, 10
	s_add_u32 s8, s6, 0x3400
	s_addc_u32 s9, s7, 0
	s_nop 2
	global_load_dword v2, v2, s[6:7] offset:1024 sc1
	s_waitcnt vmcnt(0)
	v_cmp_lt_u32_e32 vcc, v2, v3
	s_and_saveexec_b64 s[6:7], vcc
	s_cbranch_execz .LBB0_1151
	s_mov_b32 s20, 1
	s_mov_b64 s[10:11], 0
	v_mov_b32_e32 v2, 0
	s_branch .LBB0_1142

.LBB0_1146:
	global_load_dword v4, v2, s[8:9] sc1
	s_add_i32 s20, s20, 1
	s_mov_b64 s[16:17], -1
	s_waitcnt vmcnt(0)
	v_cmp_ge_u32_e32 vcc, v4, v3
	s_orn2_b64 s[14:15], vcc, exec
	s_branch .LBB0_1141

.LBB0_1251:
	s_or_b64 exec, exec, s[2:3]
	v_cvt_f32_u32_e32 v6, v4
	s_waitcnt vmcnt(0)
	v_readfirstlane_b32 s2, v5
	v_sub_u32_e32 v5, 0, v4
	v_rcp_iflag_f32_e32 v6, v6
	v_add_u32_e32 v7, s2, v3
	v_mul_f32_e32 v6, 0x4f7ffffe, v6
	v_cvt_u32_f32_e32 v6, v6
	v_mul_lo_u32 v3, v5, v6
	v_mul_hi_u32 v3, v6, v3
	v_add_u32_e32 v3, v6, v3
	v_mul_hi_u32 v3, v7, v3
	v_mul_lo_u32 v5, v3, v4
	v_sub_u32_e32 v5, v7, v5
	v_add_u32_e32 v6, 1, v3
	v_cmp_ge_u32_e32 vcc, v5, v4
	s_nop 1
	v_cndmask_b32_e32 v3, v3, v6, vcc
	v_sub_u32_e32 v6, v5, v4
	v_cndmask_b32_e32 v5, v5, v6, vcc
	v_add_u32_e32 v6, 1, v3
	v_cmp_ge_u32_e32 vcc, v5, v4
	v_add_u32_e32 v5, 1, v7
	s_nop 0
	v_cndmask_b32_e32 v3, v3, v6, vcc
	v_mul_lo_u32 v6, v4, v3
	v_add_u32_e32 v4, v6, v4
	v_cmp_ne_u32_e32 vcc, v5, v4
	s_and_saveexec_b64 s[2:3], vcc
	s_xor_b64 s[2:3], exec, s[2:3]
	s_cbranch_execz .LBB0_1265
	v_readlane_b32 s6, v255, 9
	s_waitcnt lgkmcnt(0)
	v_mov_b32_e32 v2, 0x20164
	ds_read_b32 v2, v2
	s_waitcnt lgkmcnt(0)
	v_add_u32_e32 v3, 1, v3
	v_mul_lo_u32 v3, v3, v2
	v_mov_b32_e32 v2, 0x3000
	v_readlane_b32 s7, v255, 10
	s_add_u32 s12, s6, 0x3400
	s_addc_u32 s13, s7, 0
	s_nop 2
	global_load_dword v2, v2, s[6:7] offset:1024 sc1
	s_waitcnt vmcnt(0)
	v_cmp_lt_u32_e32 vcc, v2, v3
	s_and_saveexec_b64 s[6:7], vcc
	s_cbranch_execz .LBB0_1264
	s_mov_b32 s8, 1
	s_mov_b64 s[14:15], 0
	v_mov_b32_e32 v2, 0
	s_branch .LBB0_1255

.LBB0_1259:
	global_load_dword v4, v2, s[12:13] sc1
	s_add_i32 s8, s8, 1
	s_mov_b64 s[20:21], -1
	s_waitcnt vmcnt(0)
	v_cmp_ge_u32_e32 vcc, v4, v3
	s_orn2_b64 s[18:19], vcc, exec
	s_branch .LBB0_1254

.LBB0_1360:
	s_or_b64 exec, exec, s[4:5]
	v_cvt_f32_u32_e32 v4, v2
	s_waitcnt vmcnt(0)
	v_readfirstlane_b32 s4, v3
	v_sub_u32_e32 v3, 0, v2
	v_rcp_iflag_f32_e32 v4, v4
	v_add_u32_e32 v5, s4, v1
	v_mul_f32_e32 v4, 0x4f7ffffe, v4
	v_cvt_u32_f32_e32 v4, v4
	v_mul_lo_u32 v1, v3, v4
	v_mul_hi_u32 v1, v4, v1
	v_add_u32_e32 v1, v4, v1
	v_mul_hi_u32 v1, v5, v1
	v_mul_lo_u32 v3, v1, v2
	v_sub_u32_e32 v3, v5, v3
	v_add_u32_e32 v4, 1, v1
	v_cmp_ge_u32_e32 vcc, v3, v2
	s_nop 1
	v_cndmask_b32_e32 v1, v1, v4, vcc
	v_sub_u32_e32 v4, v3, v2
	v_cndmask_b32_e32 v3, v3, v4, vcc
	v_add_u32_e32 v4, 1, v1
	v_cmp_ge_u32_e32 vcc, v3, v2
	v_add_u32_e32 v3, 1, v5
	s_nop 0
	v_cndmask_b32_e32 v1, v1, v4, vcc
	v_mul_lo_u32 v4, v2, v1
	v_add_u32_e32 v2, v4, v2
	v_cmp_ne_u32_e32 vcc, v3, v2
	s_and_saveexec_b64 s[4:5], vcc
	s_xor_b64 s[4:5], exec, s[4:5]
	s_cbranch_execz .LBB0_1374
	v_readlane_b32 s6, v255, 9
	s_waitcnt lgkmcnt(0)
	v_mov_b32_e32 v0, 0x20164
	ds_read_b32 v0, v0
	s_waitcnt lgkmcnt(0)
	v_add_u32_e32 v1, 1, v1
	v_mul_lo_u32 v1, v1, v0
	v_mov_b32_e32 v0, 0x3000
	v_readlane_b32 s7, v255, 10
	s_add_u32 s8, s6, 0x3400
	s_addc_u32 s9, s7, 0
	s_nop 2
	global_load_dword v0, v0, s[6:7] offset:1024 sc1
	s_waitcnt vmcnt(0)
	v_cmp_lt_u32_e32 vcc, v0, v1
	s_and_saveexec_b64 s[6:7], vcc
	s_cbranch_execz .LBB0_1373
	s_mov_b32 s22, 1
	s_mov_b64 s[10:11], 0
	v_mov_b32_e32 v0, 0
	s_branch .LBB0_1364

.LBB0_1368:
	global_load_dword v2, v0, s[8:9] sc1
	s_add_i32 s22, s22, 1
	s_mov_b64 s[18:19], -1
	s_waitcnt vmcnt(0)
	v_cmp_ge_u32_e32 vcc, v2, v1
	s_orn2_b64 s[16:17], vcc, exec
	s_branch .LBB0_1363
